# GLA pass 2: gate tile fetched by LDS-DMA at chunk start (no VGPRs) and read back from LDS at the output step
# baseline (speedup 1.0000x reference)
; #define GAS __attribute__((address_space(1)))
; #define LAS __attribute__((address_space(3)))
; #define GLA_FENCE() asm volatile("" ::: "memory")
; template <int PASS> ...
;     ...
;         for (int kt = 0; kt < 2; ++kt) vb[kt] = cat4(trread(vtr + kt * 32 * VS), trread(vtr + kt * 32 * VS + 4 * VS));
;         if (PASS == 2) {
;             const int it = w >> 1, jt0 = 2 * (w & 1);
;             f32x4 pa0 = (f32x4){0.f, 0.f, 0.f, 0.f}, pa1 = pa0;
;             bf16x8 fb[4], fa0[4], fa1[4];
;     ...
;             P_LOAD(0, 0); P_LOAD(1, 1); P_LOAD(2, 2);
; #pragma unroll
;             for (int ks = 0; ks < 8; ++ks) { if (ks + 3 < 8) P_LOAD((ks + 3) & 3, ks + 3); GLA_FENCE();
;                 pa0 = __builtin_amdgcn_mfma_f32_16x16x32_bf16(fa0[ks & 3], fb[ks & 3], pa0, 0, 0, 0); pa1 = __builtin_amdgcn_mfma_f32_16x16x32_bf16(fa1[ks & 3], fb[ks & 3], pa1, 0, 0, 0); }
;     ...
;             { const int i = 16 * it + r, j0 = 16 * jt0 + 4 * q; v2u o;
;               o.x = cvtpk(j0 + 0 <= i ? pa0[0] : 0.f, j0 + 1 <= i ? pa0[1] : 0.f); o.y = cvtpk(j0 + 2 <= i ? pa0[2] : 0.f, j0 + 3 <= i ? pa0[3] : 0.f);
;               *(LAS v2u*)(lds + OFF_P + i * PS + j0 * 2) = o;
;               o.x = cvtpk(j0 + 16 <= i ? pa1[0] : 0.f, j0 + 17 <= i ? pa1[1] : 0.f); o.y = cvtpk(j0 + 18 <= i ? pa1[2] : 0.f, j0 + 19 <= i ? pa1[3] : 0.f);
;               *(LAS v2u*)(lds + OFF_P + i * PS + (j0 + 16) * 2) = o; }
;             f32x4 Oa[4];
; #pragma unroll
;             for (int i4 = 0; i4 < 4; ++i4) Oa[i4] = (f32x4){0.f, 0.f, 0.f, 0.f};
;             bf16x8 qa[2][4];
;     ...
;             Q_LOAD(0, 0); GLA_FENCE();
; #pragma unroll
;             for (int ks = 0; ks < 8; ++ks) {
;                 if (ks + 1 < 8) Q_LOAD((ks + 1) & 1, ks + 1);
;                 GLA_FENCE();
;                 v4u bw; bw.x = cvtpk(S[2 * ks][0], S[2 * ks][1]); bw.y = cvtpk(S[2 * ks][2], S[2 * ks][3]); bw.z = cvtpk(S[2 * ks + 1][0], S[2 * ks + 1][1]); bw.w = cvtpk(S[2 * ks + 1][2], S[2 * ks + 1][3]);
;                 const bf16x8 bfrag = __builtin_bit_cast(bf16x8, bw);
; #pragma unroll
;                 for (int i4 = 0; i4 < 4; ++i4) Oa[i4] = __builtin_amdgcn_mfma_f32_16x16x32_bf16(bfrag, qa[ks & 1][i4], Oa[i4], 0, 0, 0);
;             }
;     ...
;             for (int i = 0; i < 2; ++i) gpre[i] = *(const GAS v4u*)((const GAS char*)GB + (size_t)tok0 * VD * 2 + i * 32 * VD * 2 + voff);
.LBB0_424:
	v_add_u32_e32 v170, s73, v222
	ds_read_b64_tr_b16 v[106:107], v187
	ds_read_b64_tr_b16 v[108:109], v187 offset:1152
	ds_read_b64_tr_b16 v[110:111], v187 offset:9216
	ds_read_b64_tr_b16 v[112:113], v187 offset:10368
	s_waitcnt vmcnt(11)
	s_lshl_b32 s98, s33, 10
	s_add_i32 s98, s98, 0x1c000
	v_add_co_u32_e32 v254, vcc, s88, v208
	s_mov_b32 m0, s98
	s_nop 1
	v_addc_co_u32_e32 v255, vcc, -1, v209, vcc
	global_load_lds_dwordx4 v[254:255], off
	v_add_co_u32_e32 v254, vcc, s89, v208
	s_add_i32 m0, s98, 0x2000
	s_nop 1
	v_addc_co_u32_e32 v255, vcc, -1, v209, vcc
	global_load_lds_dwordx4 v[254:255], off
	ds_read_b128 v[114:117], v170
	ds_read_b128 v[118:121], v189 offset:33792
	ds_read_b128 v[122:125], v189 offset:42496
	ds_read_b128 v[126:129], v170 offset:64
	ds_read_b128 v[130:133], v189 offset:33856
	ds_read_b128 v[134:137], v189 offset:42560
	ds_read_b128 v[138:141], v170 offset:128
	ds_read_b128 v[142:145], v226 offset:33920
	ds_read_b128 v[146:149], v226 offset:42624
	ds_read_b128 v[150:153], v170 offset:192
	ds_read_b128 v[154:157], v226 offset:33984
	ds_read_b128 v[158:161], v226 offset:42688
	s_waitcnt lgkmcnt(10)
	v_mfma_f32_16x16x32_bf16 v[118:121], v[118:121], v[114:117], 0
	v_and_b32_e32 v202, 64, v244
	v_xor_b32_e32 v190, 1, v244
	s_waitcnt lgkmcnt(9)
	v_mfma_f32_16x16x32_bf16 v[114:117], v[122:125], v[114:117], 0
	ds_read_b128 v[122:125], v170 offset:256
	ds_read_b128 v[162:165], v189 offset:34048
	ds_read_b128 v[166:169], v189 offset:42752
	s_waitcnt lgkmcnt(10)
	v_mfma_f32_16x16x32_bf16 v[118:121], v[130:133], v[126:129], v[118:121]
	s_waitcnt lgkmcnt(9)
	v_mfma_f32_16x16x32_bf16 v[114:117], v[134:137], v[126:129], v[114:117]
	ds_read_b128 v[126:129], v170 offset:320
	ds_read_b128 v[130:133], v189 offset:34112
	ds_read_b128 v[134:137], v189 offset:42816
	s_waitcnt lgkmcnt(10)
	v_mfma_f32_16x16x32_bf16 v[118:121], v[142:145], v[138:141], v[118:121]
	s_waitcnt lgkmcnt(9)
	v_mfma_f32_16x16x32_bf16 v[114:117], v[146:149], v[138:141], v[114:117]
	ds_read_b128 v[138:141], v170 offset:384
	ds_read_b128 v[142:145], v226 offset:34176
	ds_read_b128 v[146:149], v226 offset:42880
	s_waitcnt lgkmcnt(10)
	v_mfma_f32_16x16x32_bf16 v[118:121], v[154:157], v[150:153], v[118:121]
	s_waitcnt lgkmcnt(9)
	v_mfma_f32_16x16x32_bf16 v[114:117], v[158:161], v[150:153], v[114:117]
	ds_read_b128 v[150:153], v170 offset:448
	ds_read_b128 v[154:157], v226 offset:34240
	ds_read_b128 v[158:161], v226 offset:42944
	s_waitcnt lgkmcnt(10)
	v_mfma_f32_16x16x32_bf16 v[118:121], v[162:165], v[122:125], v[118:121]
	v_cvt_pk_bf16_f32 v162, v94, v95
	s_waitcnt lgkmcnt(9)
	v_mfma_f32_16x16x32_bf16 v[114:117], v[166:169], v[122:125], v[114:117]
	v_cvt_pk_bf16_f32 v163, v96, v97
	v_cvt_pk_bf16_f32 v164, v90, v91
	v_cvt_pk_bf16_f32 v165, v92, v93
	s_waitcnt lgkmcnt(7)
	v_mfma_f32_16x16x32_bf16 v[118:121], v[130:133], v[126:129], v[118:121]
	v_add_u32_e32 v166, v225, v224
	s_waitcnt lgkmcnt(6)
	v_mfma_f32_16x16x32_bf16 v[114:117], v[134:137], v[126:129], v[114:117]
	s_waitcnt lgkmcnt(4)
	v_mfma_f32_16x16x32_bf16 v[118:121], v[142:145], v[138:141], v[118:121]
	s_waitcnt lgkmcnt(3)
	v_mfma_f32_16x16x32_bf16 v[114:117], v[146:149], v[138:141], v[114:117]
	v_cvt_pk_bf16_f32 v146, v102, v103
	v_cvt_pk_bf16_f32 v147, v104, v105
	v_cvt_pk_bf16_f32 v148, v98, v99
	s_waitcnt lgkmcnt(1)
	v_mfma_f32_16x16x32_bf16 v[118:121], v[154:157], v[150:153], v[118:121]
	v_cvt_pk_bf16_f32 v149, v100, v101
	s_waitcnt lgkmcnt(0)
	v_mfma_f32_16x16x32_bf16 v[114:117], v[158:161], v[150:153], v[114:117]
	s_nop 4
	v_cndmask_b32_e64 v118, v118, 0, s[10:11]
	v_cndmask_b32_e64 v119, 0, v119, s[12:13]
	s_nop 0
	v_cndmask_b32_e64 v114, v114, 0, s[18:19]
	v_cndmask_b32_e64 v115, v115, 0, s[20:21]
	v_cvt_pk_bf16_f32 v118, v118, v119
	v_cndmask_b32_e64 v119, v120, 0, s[14:15]
	v_cndmask_b32_e64 v120, v121, 0, s[16:17]
	v_cvt_pk_bf16_f32 v114, v114, v115
	v_cndmask_b32_e64 v115, v116, 0, s[22:23]
	v_cndmask_b32_e64 v116, v117, 0, s[24:25]
	v_cvt_pk_bf16_f32 v119, v119, v120
	v_cvt_pk_bf16_f32 v115, v115, v116
	ds_write_b64 v227, v[118:119]
	ds_write_b64 v228, v[114:115]
	ds_read_b64 v[126:127], v223
	ds_read_b64 v[128:129], v246
	ds_read_b64 v[130:131], v223 offset:8448
	ds_read_b64 v[132:133], v246 offset:8448
	ds_read_b64 v[134:135], v223 offset:16896
	ds_read_b64 v[136:137], v246 offset:16896
	ds_read_b64 v[138:139], v223 offset:25344
	ds_read_b64 v[140:141], v246 offset:25344
	ds_read_b64 v[142:143], v223 offset:64
	ds_read_b64 v[144:145], v246 offset:64
	ds_read_b64 v[122:123], v223 offset:8512
	ds_read_b64 v[124:125], v246 offset:8512
	ds_read_b64 v[114:115], v223 offset:16960
	ds_read_b64 v[116:117], v246 offset:16960
	ds_read_b64 v[118:119], v223 offset:25408
	ds_read_b64 v[120:121], v246 offset:25408
	s_waitcnt lgkmcnt(14)
	v_mfma_f32_16x16x32_bf16 v[126:129], v[146:149], v[126:129], 0
	s_waitcnt lgkmcnt(12)
	v_mfma_f32_16x16x32_bf16 v[130:133], v[146:149], v[130:133], 0
	s_waitcnt lgkmcnt(10)
	v_mfma_f32_16x16x32_bf16 v[134:137], v[146:149], v[134:137], 0
	s_waitcnt lgkmcnt(8)
	v_mfma_f32_16x16x32_bf16 v[138:141], v[146:149], v[138:141], 0
	ds_read_b64 v[146:147], v223 offset:128
	ds_read_b64 v[148:149], v246 offset:128
	ds_read_b64 v[150:151], v223 offset:8576
	ds_read_b64 v[152:153], v246 offset:8576
	ds_read_b64 v[154:155], v223 offset:17024
	ds_read_b64 v[156:157], v246 offset:17024
	ds_read_b64 v[158:159], v223 offset:25472
	ds_read_b64 v[160:161], v246 offset:25472
	s_waitcnt lgkmcnt(14)
	v_mfma_f32_16x16x32_bf16 v[126:129], v[162:165], v[142:145], v[126:129]
	s_waitcnt lgkmcnt(12)
	v_mfma_f32_16x16x32_bf16 v[122:125], v[162:165], v[122:125], v[130:133]
	s_waitcnt lgkmcnt(10)
; __device__ __forceinline__ unsigned cvtpk(float lo, float hi) { f32x2_t v = {lo, hi}; bf16x2_t b = __builtin_convertvector(v, bf16x2_t); return __builtin_bit_cast(unsigned, b); }
; #define GLA_FENCE() asm volatile("" ::: "memory")
; #define GLA_BAR() do { asm volatile("s_waitcnt lgkmcnt(0)" ::: "memory"); __builtin_amdgcn_s_barrier(); asm volatile("" ::: "memory"); } while (0)
; #define Q_LOAD(sl, ks) do { _Pragma("unroll") for (int i4 = 0; i4 < 4; ++i4) qa[sl][i4] = cat4(*(const LAS s16x4*)(qperm + i4 * 16 * QS + (ks) * 64), *(const LAS s16x4*)(qperm2 + i4 * 16 * QS + (ks) * 64)); } while (0)
; template <int PASS> ...
;     ...
;             for (int ks = 0; ks < 8; ++ks) {
;                 if (ks + 1 < 8) Q_LOAD((ks + 1) & 1, ks + 1);
;                 GLA_FENCE();
;                 v4u bw; bw.x = cvtpk(S[2 * ks][0], S[2 * ks][1]); bw.y = cvtpk(S[2 * ks][2], S[2 * ks][3]); bw.z = cvtpk(S[2 * ks + 1][0], S[2 * ks + 1][1]); bw.w = cvtpk(S[2 * ks + 1][2], S[2 * ks + 1][3]);
;                 const bf16x8 bfrag = __builtin_bit_cast(bf16x8, bw);
; #pragma unroll
;                 for (int i4 = 0; i4 < 4; ++i4) Oa[i4] = __builtin_amdgcn_mfma_f32_16x16x32_bf16(bfrag, qa[ks & 1][i4], Oa[i4], 0, 0, 0);
;             }
;     ...
;             GLA_BAR();
	v_mfma_f32_16x16x32_bf16 v[114:117], v[162:165], v[114:117], v[134:137]
	s_waitcnt lgkmcnt(8)
	v_mfma_f32_16x16x32_bf16 v[118:121], v[162:165], v[118:121], v[138:141]
	v_cvt_pk_bf16_f32 v162, v70, v71
	v_cvt_pk_bf16_f32 v163, v72, v73
	v_cvt_pk_bf16_f32 v164, v54, v55
	v_cvt_pk_bf16_f32 v165, v56, v57
	ds_read_b64 v[130:131], v223 offset:192
	ds_read_b64 v[132:133], v246 offset:192
	ds_read_b64 v[134:135], v223 offset:8640
	ds_read_b64 v[136:137], v246 offset:8640
	ds_read_b64 v[138:139], v223 offset:17088
	ds_read_b64 v[140:141], v246 offset:17088
	ds_read_b64 v[142:143], v223 offset:25536
	ds_read_b64 v[144:145], v246 offset:25536
	s_waitcnt lgkmcnt(14)
	v_mfma_f32_16x16x32_bf16 v[126:129], v[162:165], v[146:149], v[126:129]
	s_waitcnt lgkmcnt(12)
	v_mfma_f32_16x16x32_bf16 v[122:125], v[162:165], v[150:153], v[122:125]
	s_waitcnt lgkmcnt(10)
	v_mfma_f32_16x16x32_bf16 v[114:117], v[162:165], v[154:157], v[114:117]
	s_waitcnt lgkmcnt(8)
	v_mfma_f32_16x16x32_bf16 v[118:121], v[162:165], v[158:161], v[118:121]
	v_cvt_pk_bf16_f32 v162, v38, v39
	v_cvt_pk_bf16_f32 v163, v40, v41
	v_cvt_pk_bf16_f32 v164, v34, v35
	v_cvt_pk_bf16_f32 v165, v36, v37
	ds_read_b64 v[146:147], v223 offset:256
	ds_read_b64 v[148:149], v246 offset:256
	ds_read_b64 v[150:151], v223 offset:8704
	ds_read_b64 v[152:153], v246 offset:8704
	ds_read_b64 v[154:155], v223 offset:17152
	ds_read_b64 v[156:157], v246 offset:17152
	ds_read_b64 v[158:159], v223 offset:25600
	ds_read_b64 v[160:161], v246 offset:25600
	s_waitcnt lgkmcnt(14)
	v_mfma_f32_16x16x32_bf16 v[126:129], v[162:165], v[130:133], v[126:129]
	s_waitcnt lgkmcnt(12)
	v_mfma_f32_16x16x32_bf16 v[122:125], v[162:165], v[134:137], v[122:125]
	s_waitcnt lgkmcnt(10)
	v_mfma_f32_16x16x32_bf16 v[114:117], v[162:165], v[138:141], v[114:117]
	s_waitcnt lgkmcnt(8)
	v_mfma_f32_16x16x32_bf16 v[118:121], v[162:165], v[142:145], v[118:121]
	v_cvt_pk_bf16_f32 v162, v30, v31
	v_cvt_pk_bf16_f32 v163, v32, v33
	v_cvt_pk_bf16_f32 v164, v26, v27
	v_cvt_pk_bf16_f32 v165, v28, v29
	ds_read_b64 v[130:131], v223 offset:320
	ds_read_b64 v[132:133], v246 offset:320
	ds_read_b64 v[134:135], v223 offset:8768
	ds_read_b64 v[136:137], v246 offset:8768
	ds_read_b64 v[138:139], v223 offset:17216
	ds_read_b64 v[140:141], v246 offset:17216
	ds_read_b64 v[142:143], v223 offset:25664
	ds_read_b64 v[144:145], v246 offset:25664
	s_waitcnt lgkmcnt(14)
	v_mfma_f32_16x16x32_bf16 v[126:129], v[162:165], v[146:149], v[126:129]
	s_waitcnt lgkmcnt(12)
	v_mfma_f32_16x16x32_bf16 v[122:125], v[162:165], v[150:153], v[122:125]
	s_waitcnt lgkmcnt(10)
	v_mfma_f32_16x16x32_bf16 v[114:117], v[162:165], v[154:157], v[114:117]
	s_waitcnt lgkmcnt(8)
	v_mfma_f32_16x16x32_bf16 v[118:121], v[162:165], v[158:161], v[118:121]
	v_cvt_pk_bf16_f32 v162, v22, v23
	v_cvt_pk_bf16_f32 v163, v24, v25
	v_cvt_pk_bf16_f32 v164, v18, v19
	v_cvt_pk_bf16_f32 v165, v20, v21
	ds_read_b64 v[146:147], v223 offset:384
	ds_read_b64 v[148:149], v246 offset:384
	ds_read_b64 v[150:151], v223 offset:8832
	ds_read_b64 v[152:153], v246 offset:8832
	ds_read_b64 v[154:155], v223 offset:17280
	ds_read_b64 v[156:157], v246 offset:17280
	ds_read_b64 v[158:159], v223 offset:25728
	ds_read_b64 v[160:161], v246 offset:25728
	s_waitcnt lgkmcnt(14)
	v_mfma_f32_16x16x32_bf16 v[126:129], v[162:165], v[130:133], v[126:129]
	s_waitcnt lgkmcnt(12)
	v_mfma_f32_16x16x32_bf16 v[122:125], v[162:165], v[134:137], v[122:125]
	s_waitcnt lgkmcnt(10)
	v_mfma_f32_16x16x32_bf16 v[114:117], v[162:165], v[138:141], v[114:117]
	s_waitcnt lgkmcnt(8)
	v_mfma_f32_16x16x32_bf16 v[118:121], v[162:165], v[142:145], v[118:121]
	v_cvt_pk_bf16_f32 v162, v14, v15
	v_cvt_pk_bf16_f32 v163, v16, v17
	v_cvt_pk_bf16_f32 v164, v10, v11
	v_cvt_pk_bf16_f32 v165, v12, v13
	ds_read_b64 v[130:131], v223 offset:448
	ds_read_b64 v[132:133], v246 offset:448
	ds_read_b64 v[134:135], v223 offset:8896
	ds_read_b64 v[136:137], v246 offset:8896
	ds_read_b64 v[138:139], v223 offset:17344
	ds_read_b64 v[140:141], v246 offset:17344
	ds_read_b64 v[142:143], v223 offset:25792
	ds_read_b64 v[144:145], v246 offset:25792
	s_waitcnt lgkmcnt(14)
	v_mfma_f32_16x16x32_bf16 v[126:129], v[162:165], v[146:149], v[126:129]
	v_cvt_pk_bf16_f32 v146, v6, v7
	v_cvt_pk_bf16_f32 v147, v8, v9
	v_cvt_pk_bf16_f32 v148, v2, v3
	v_cvt_pk_bf16_f32 v149, v4, v5
	s_waitcnt lgkmcnt(12)
	v_mfma_f32_16x16x32_bf16 v[122:125], v[162:165], v[150:153], v[122:125]
	s_waitcnt lgkmcnt(0)
	s_waitcnt lgkmcnt(10)
	v_mfma_f32_16x16x32_bf16 v[114:117], v[162:165], v[154:157], v[114:117]
	s_barrier
; #define GAS __attribute__((address_space(1)))
; #define LAS __attribute__((address_space(3)))
; __device__ __forceinline__ unsigned cvtpk(float lo, float hi) { f32x2_t v = {lo, hi}; bf16x2_t b = __builtin_convertvector(v, bf16x2_t); return __builtin_bit_cast(unsigned, b); }
; #define GTP_BEGIN(k) do { if ((TPROBE_MASK >> (k)) & 1u) { if (tid == 0) ((volatile LAS int*)(lds + MISC_OFF))[50] = (int)__builtin_amdgcn_s_memrealtime(); } } while (0)
; #define GLA_FENCE() asm volatile("" ::: "memory")
; template <int PASS> ...
;     ...
;             for (int i = 0; i < 2; ++i) gpre[i] = *(const GAS v4u*)((const GAS char*)GB + (size_t)tok0 * VD * 2 + i * 32 * VD * 2 + voff);
;             { bf16x8 pf[6];
;               pf[0] = *(const LAS bf16x8*)(pnat); pf[1] = *(const LAS bf16x8*)(pnat + 16 * PS); pf[2] = *(const LAS bf16x8*)(pnat + 32 * PS); pf[3] = *(const LAS bf16x8*)(pnat + 32 * PS + 64);
;               pf[4] = *(const LAS bf16x8*)(pnat + 48 * PS); pf[5] = *(const LAS bf16x8*)(pnat + 48 * PS + 64);
;               Oa[0] = __builtin_amdgcn_mfma_f32_16x16x32_bf16(vb[0], pf[0], Oa[0], 0, 0, 0); Oa[1] = __builtin_amdgcn_mfma_f32_16x16x32_bf16(vb[0], pf[1], Oa[1], 0, 0, 0);
;               Oa[2] = __builtin_amdgcn_mfma_f32_16x16x32_bf16(vb[0], pf[2], Oa[2], 0, 0, 0); Oa[2] = __builtin_amdgcn_mfma_f32_16x16x32_bf16(vb[1], pf[3], Oa[2], 0, 0, 0);
;               Oa[3] = __builtin_amdgcn_mfma_f32_16x16x32_bf16(vb[0], pf[4], Oa[3], 0, 0, 0); Oa[3] = __builtin_amdgcn_mfma_f32_16x16x32_bf16(vb[1], pf[5], Oa[3], 0, 0, 0); }
; #pragma unroll
;             for (int i4 = 0; i4 < 4; ++i4) { v2u o; o.x = cvtpk(Oa[i4][0], Oa[i4][1]); o.y = cvtpk(Oa[i4][2], Oa[i4][3]); *(LAS v2u*)(lds + OFF_O + (16 * i4 + r) * OS + (16 * w + 4 * q) * 2) = o; }
;         }
;         if (PASS == 2) { GTP_END(25); GTP_BEGIN(26); }
;         { constexpr int RD = (PASS == 1) ? 4 : 2;
;           bf16x8 ka0[RD], ka1[RD]; f32x4 gg[RD];
;     ...
; #pragma unroll
;           for (int d0 = 0; d0 < RD - 1; ++d0) KV_LOAD(d0, d0);
; #pragma unroll
;           for (int dt = 0; dt < 16; ++dt) { if (dt + RD - 1 < 16) KV_LOAD((dt + RD - 1) % RD, dt + RD - 1); GLA_FENCE();
;               S[dt] = __builtin_amdgcn_mfma_f32_16x16x32_bf16(ka0[dt % RD], vb[0], S[dt], 0, 0, 0); S[dt] = __builtin_amdgcn_mfma_f32_16x16x32_bf16(ka1[dt % RD], vb[1], S[dt], 0, 0, 0);
;               S[dt] = S[dt] * gg[dt % RD]; }
	s_waitcnt lgkmcnt(8)
	v_mfma_f32_16x16x32_bf16 v[118:121], v[162:165], v[158:161], v[118:121]
	s_waitcnt lgkmcnt(6)
	v_mfma_f32_16x16x32_bf16 v[130:133], v[146:149], v[130:133], v[126:129]
	s_nop 2
	v_add_co_u32_e32 v126, vcc, s88, v208
	s_waitcnt lgkmcnt(4)
	v_mfma_f32_16x16x32_bf16 v[122:125], v[146:149], v[134:137], v[122:125]
	v_addc_co_u32_e32 v127, vcc, -1, v209, vcc
	s_waitcnt lgkmcnt(2)
	v_mfma_f32_16x16x32_bf16 v[114:117], v[146:149], v[138:141], v[114:117]
	s_waitcnt lgkmcnt(0)
	v_mfma_f32_16x16x32_bf16 v[118:121], v[146:149], v[142:145], v[118:121]
	s_nop 0
	v_add_co_u32_e32 v126, vcc, s89, v208
	s_nop 1
	v_addc_co_u32_e32 v127, vcc, -1, v209, vcc
	s_nop 0
	ds_read_b128 v[134:137], v229
	ds_read_b128 v[138:141], v229 offset:2304
	ds_read_b128 v[142:145], v229 offset:4608
	ds_read_b128 v[150:153], v229 offset:4672
	ds_read_b128 v[154:157], v229 offset:6912
	ds_read_b128 v[158:161], v229 offset:6976
	s_waitcnt lgkmcnt(3)
	v_mfma_f32_16x16x32_bf16 v[114:117], v[106:109], v[142:145], v[114:117]
	s_waitcnt lgkmcnt(1)
	v_mfma_f32_16x16x32_bf16 v[118:121], v[106:109], v[154:157], v[118:121]
	v_mfma_f32_16x16x32_bf16 v[114:117], v[110:113], v[150:153], v[114:117]
	v_mfma_f32_16x16x32_bf16 v[130:133], v[106:109], v[134:137], v[130:133]
	v_mfma_f32_16x16x32_bf16 v[122:125], v[106:109], v[138:141], v[122:125]
	s_nop 5
	v_cvt_pk_bf16_f32 v114, v114, v115
	v_cvt_pk_bf16_f32 v115, v116, v117
	v_cvt_pk_bf16_f32 v130, v130, v131
	s_waitcnt lgkmcnt(0)
	v_mfma_f32_16x16x32_bf16 v[118:121], v[110:113], v[158:161], v[118:121]
	v_cvt_pk_bf16_f32 v131, v132, v133
	v_cvt_pk_bf16_f32 v122, v122, v123
	v_cvt_pk_bf16_f32 v123, v124, v125
	ds_write_b64 v230, v[114:115] offset:8704
	ds_write_b64 v230, v[130:131]
	s_nop 2
	v_cvt_pk_bf16_f32 v114, v118, v119
	v_cvt_pk_bf16_f32 v115, v120, v121
	ds_write_b64 v230, v[122:123] offset:4352
	ds_write_b64 v230, v[114:115] offset:13056
	ds_read_b64_tr_b16 v[124:125], v166 offset:35968
	ds_read_b64_tr_b16 v[130:131], v166 offset:51200
	ds_read_b64_tr_b16 v[132:133], v166 offset:53376
	ds_read_b64_tr_b16 v[122:123], v166 offset:33792
	ds_read_b64_tr_b16 v[134:135], v166 offset:33824
	v_add_u32_e32 v114, 0, v221
	v_add_u32_e32 v182, 0x17800, v114
	ds_read_b128 v[114:117], v182
	ds_read_b64_tr_b16 v[136:137], v166 offset:36000
	ds_read_b64_tr_b16 v[138:139], v166 offset:51232
	ds_read_b64_tr_b16 v[140:141], v166 offset:53408
	ds_read_b128 v[118:121], v182 offset:64
	s_waitcnt lgkmcnt(6)
	v_mfma_f32_16x16x32_bf16 v[102:105], v[122:125], v[106:109], v[102:105]
	ds_read_b64_tr_b16 v[142:143], v166 offset:33856
	ds_read_b64_tr_b16 v[144:145], v166 offset:36032
	ds_read_b64_tr_b16 v[150:151], v166 offset:51264
	ds_read_b64_tr_b16 v[152:153], v166 offset:53440
	ds_read_b128 v[122:125], v182 offset:128
	s_waitcnt lgkmcnt(8)
	v_mfma_f32_16x16x32_bf16 v[98:101], v[134:137], v[106:109], v[98:101]
	v_mfma_f32_16x16x32_bf16 v[102:105], v[130:133], v[110:113], v[102:105]
	s_waitcnt lgkmcnt(6)
	v_mfma_f32_16x16x32_bf16 v[98:101], v[138:141], v[110:113], v[98:101]
	ds_read_b64_tr_b16 v[138:139], v166 offset:33888
	ds_read_b64_tr_b16 v[140:141], v166 offset:36064
	ds_read_b64_tr_b16 v[154:155], v166 offset:51296
	ds_read_b64_tr_b16 v[156:157], v166 offset:53472
	ds_read_b128 v[130:133], v182 offset:192
	s_waitcnt lgkmcnt(8)
	v_mfma_f32_16x16x32_bf16 v[94:97], v[142:145], v[106:109], v[94:97]
	s_waitcnt lgkmcnt(3)
	v_mfma_f32_16x16x32_bf16 v[90:93], v[138:141], v[106:109], v[90:93]
	v_mfma_f32_16x16x32_bf16 v[94:97], v[150:153], v[110:113], v[94:97]
	ds_read_b64_tr_b16 v[142:143], v231 offset:33920
	ds_read_b64_tr_b16 v[144:145], v231 offset:36096
	ds_read_b64_tr_b16 v[150:151], v231 offset:51328
	ds_read_b64_tr_b16 v[152:153], v231 offset:53504
	ds_read_b128 v[134:137], v182 offset:256
	s_waitcnt lgkmcnt(6)
	v_mfma_f32_16x16x32_bf16 v[90:93], v[154:157], v[110:113], v[90:93]
	ds_read_b64_tr_b16 v[154:155], v231 offset:33952
	ds_read_b64_tr_b16 v[156:157], v231 offset:36128
	ds_read_b64_tr_b16 v[158:159], v231 offset:51360
	ds_read_b64_tr_b16 v[160:161], v231 offset:53536
	ds_read_b128 v[138:141], v182 offset:320
	s_waitcnt lgkmcnt(8)
	v_mfma_f32_16x16x32_bf16 v[70:73], v[142:145], v[106:109], v[70:73]
	ds_read_b64_tr_b16 v[162:163], v231 offset:33984
	ds_read_b64_tr_b16 v[164:165], v231 offset:36160
	ds_read_b64_tr_b16 v[168:169], v231 offset:51392
	ds_read_b64_tr_b16 v[170:171], v231 offset:53568
	ds_read_b128 v[142:145], v182 offset:384
	s_waitcnt lgkmcnt(8)
	v_mfma_f32_16x16x32_bf16 v[54:57], v[154:157], v[106:109], v[54:57]
	v_mfma_f32_16x16x32_bf16 v[70:73], v[150:153], v[110:113], v[70:73]
	s_waitcnt lgkmcnt(6)
	v_mfma_f32_16x16x32_bf16 v[54:57], v[158:161], v[110:113], v[54:57]
	ds_read_b64_tr_b16 v[158:159], v231 offset:34016
	ds_read_b64_tr_b16 v[160:161], v231 offset:36192
	ds_read_b64_tr_b16 v[172:173], v231 offset:51424
	ds_read_b64_tr_b16 v[174:175], v231 offset:53600
	ds_read_b128 v[150:153], v182 offset:448
	s_waitcnt lgkmcnt(8)
	v_mfma_f32_16x16x32_bf16 v[38:41], v[162:165], v[106:109], v[38:41]
	s_waitcnt lgkmcnt(3)
	v_mfma_f32_16x16x32_bf16 v[34:37], v[158:161], v[106:109], v[34:37]
	v_mfma_f32_16x16x32_bf16 v[38:41], v[168:171], v[110:113], v[38:41]
	ds_read_b64_tr_b16 v[162:163], v166 offset:34048
	ds_read_b64_tr_b16 v[164:165], v166 offset:36224
	ds_read_b64_tr_b16 v[168:169], v166 offset:51456
	ds_read_b64_tr_b16 v[170:171], v166 offset:53632
	ds_read_b128 v[154:157], v182 offset:512
	s_waitcnt lgkmcnt(6)
	v_mfma_f32_16x16x32_bf16 v[34:37], v[172:175], v[110:113], v[34:37]
	ds_read_b64_tr_b16 v[172:173], v166 offset:34080
	ds_read_b64_tr_b16 v[174:175], v166 offset:36256
	ds_read_b64_tr_b16 v[176:177], v166 offset:51488
	ds_read_b64_tr_b16 v[178:179], v166 offset:53664
	ds_read_b128 v[158:161], v182 offset:576
	s_waitcnt lgkmcnt(8)
; #define LAS __attribute__((address_space(3)))
; __device__ __forceinline__ f32x4 bf4lo(const v4u& w) { return (f32x4){bflo(w.x), bfhi(w.x), bflo(w.y), bfhi(w.y)}; }
; __device__ __forceinline__ f32x4 bf4hi(const v4u& w) { return (f32x4){bflo(w.z), bfhi(w.z), bflo(w.w), bfhi(w.w)}; }
; #define GTP_BEGIN(k) do { if ((TPROBE_MASK >> (k)) & 1u) { if (tid == 0) ((volatile LAS int*)(lds + MISC_OFF))[50] = (int)__builtin_amdgcn_s_memrealtime(); } } while (0)
; #define GTP_END(k) do { if ((TPROBE_MASK >> (k)) & 1u) { if (tid == 0) { volatile LAS int* m_ = (volatile LAS int*)(lds + MISC_OFF); m_[51] = m_[51] + ((int)__builtin_amdgcn_s_memrealtime() - m_[50]); } } } while (0)
; #define GLA_FENCE() asm volatile("" ::: "memory")
; #define GLA_BAR() do { asm volatile("s_waitcnt lgkmcnt(0)" ::: "memory"); __builtin_amdgcn_s_barrier(); asm volatile("" ::: "memory"); } while (0)
; template <int PASS> ...
;     ...
;           for (int dt = 0; dt < 16; ++dt) { if (dt + RD - 1 < 16) KV_LOAD((dt + RD - 1) % RD, dt + RD - 1); GLA_FENCE();
;               S[dt] = __builtin_amdgcn_mfma_f32_16x16x32_bf16(ka0[dt % RD], vb[0], S[dt], 0, 0, 0); S[dt] = __builtin_amdgcn_mfma_f32_16x16x32_bf16(ka1[dt % RD], vb[1], S[dt], 0, 0, 0);
;               S[dt] = S[dt] * gg[dt % RD]; }
;     ...
;         }
;         if (PASS == 2) { GTP_END(26); GTP_BEGIN(27); }
;         GLA_BAR();
;         if (PASS == 2) {
;             const f32x4 hw0 = *(const LAS f32x4*)(lds + MISC_OFF + 256 + (tid & 15) * 32), hw1 = *(const LAS f32x4*)(lds + MISC_OFF + 256 + (tid & 15) * 32 + 16);
; #pragma unroll
;             for (int i = 0; i < 2; ++i) { const int id = tid + 512 * i, row = id >> 4, cc = id & 15;
;                 const v4u ov = *(const LAS v4u*)(lds + OFF_O + row * OS + cc * 16);
;                 const f32x4 a = bf4lo(ov), b = bf4hi(ov), ga = bf4lo(gpre[i]), gb = bf4hi(gpre[i]);
;                 float ss = (a.x * a.x + a.y * a.y) + (a.z * a.z + a.w * a.w) + (b.x * b.x + b.y * b.y) + (b.z * b.z + b.w * b.w);
;                 ss += __shfl_xor(ss, 1); ss += __shfl_xor(ss, 2); ss += __shfl_xor(ss, 4); ss += __shfl_xor(ss, 8);
;                 if (cc == 0) SS[(size_t)(tok0 + row) * 16 + h * 4 + s] = ss;
	v_mfma_f32_16x16x32_bf16 v[30:33], v[162:165], v[106:109], v[30:33]
	ds_read_b64_tr_b16 v[210:211], v166 offset:34112
	ds_read_b64_tr_b16 v[212:213], v166 offset:36288
	ds_read_b64_tr_b16 v[214:215], v166 offset:51520
	ds_read_b64_tr_b16 v[216:217], v166 offset:53696
	ds_read_b128 v[162:165], v182 offset:640
	s_waitcnt lgkmcnt(8)
	v_mfma_f32_16x16x32_bf16 v[26:29], v[172:175], v[106:109], v[26:29]
	s_waitcnt lgkmcnt(3)
	v_mfma_f32_16x16x32_bf16 v[22:25], v[210:213], v[106:109], v[22:25]
	v_mfma_f32_16x16x32_bf16 v[30:33], v[168:171], v[110:113], v[30:33]
	v_mfma_f32_16x16x32_bf16 v[26:29], v[176:179], v[110:113], v[26:29]
	ds_read_b64_tr_b16 v[174:175], v166 offset:34144
	ds_read_b64_tr_b16 v[176:177], v166 offset:36320
	ds_read_b64_tr_b16 v[178:179], v166 offset:51552
	ds_read_b64_tr_b16 v[180:181], v166 offset:53728
	ds_read_b128 v[166:169], v182 offset:704
	s_waitcnt lgkmcnt(6)
	v_mfma_f32_16x16x32_bf16 v[22:25], v[214:217], v[110:113], v[22:25]
	ds_read_b64_tr_b16 v[210:211], v231 offset:34176
	ds_read_b64_tr_b16 v[212:213], v231 offset:36352
	ds_read_b64_tr_b16 v[214:215], v231 offset:51584
	ds_read_b64_tr_b16 v[216:217], v231 offset:53760
	ds_read_b128 v[170:173], v182 offset:768
	s_waitcnt lgkmcnt(8)
	v_mfma_f32_16x16x32_bf16 v[18:21], v[174:177], v[106:109], v[18:21]
	ds_read_b64_tr_b16 v[248:249], v231 offset:34208
	ds_read_b64_tr_b16 v[250:251], v231 offset:36384
	ds_read_b64_tr_b16 v[252:253], v231 offset:51616
	ds_read_b64_tr_b16 v[254:255], v231 offset:53792
	ds_read_b128 v[174:177], v182 offset:832
	s_waitcnt lgkmcnt(8)
	v_mfma_f32_16x16x32_bf16 v[14:17], v[210:213], v[106:109], v[14:17]
	s_waitcnt lgkmcnt(3)
	v_mfma_f32_16x16x32_bf16 v[10:13], v[248:251], v[106:109], v[10:13]
	v_mfma_f32_16x16x32_bf16 v[18:21], v[178:181], v[110:113], v[18:21]
	v_mfma_f32_16x16x32_bf16 v[14:17], v[214:217], v[110:113], v[14:17]
	ds_read_b64_tr_b16 v[210:211], v231 offset:34240
	ds_read_b64_tr_b16 v[212:213], v231 offset:36416
	ds_read_b64_tr_b16 v[214:215], v231 offset:51648
	ds_read_b64_tr_b16 v[216:217], v231 offset:53824
	ds_read_b128 v[178:181], v182 offset:896
	s_waitcnt lgkmcnt(6)
	v_mfma_f32_16x16x32_bf16 v[10:13], v[252:255], v[110:113], v[10:13]
	ds_read_b64_tr_b16 v[248:249], v231 offset:34272
	ds_read_b64_tr_b16 v[250:251], v231 offset:36448
	ds_read_b64_tr_b16 v[252:253], v231 offset:51680
	ds_read_b64_tr_b16 v[254:255], v231 offset:53856
	ds_read_b128 v[182:185], v182 offset:960
	s_waitcnt lgkmcnt(8)
	v_mfma_f32_16x16x32_bf16 v[6:9], v[210:213], v[106:109], v[6:9]
	v_add_u32_e32 v210, 64, v202
	s_waitcnt lgkmcnt(0)
	s_barrier
	s_waitcnt lgkmcnt(3)
	v_mfma_f32_16x16x32_bf16 v[2:5], v[248:251], v[106:109], v[2:5]
	v_cmp_lt_i32_e32 vcc, v190, v210
	v_mfma_f32_16x16x32_bf16 v[6:9], v[214:217], v[110:113], v[6:9]
	s_nop 0
	v_cndmask_b32_e32 v190, v244, v190, vcc
	v_lshlrev_b32_e32 v249, 2, v190
	v_xor_b32_e32 v190, 2, v244
	s_waitcnt lgkmcnt(1)
	v_mfma_f32_16x16x32_bf16 v[2:5], v[252:255], v[110:113], v[2:5]
	ds_read_b128 v[110:113], v232
	ds_read_b128 v[106:109], v232 offset:16
	ds_read_b128 v[250:253], v233
	v_cmp_lt_i32_e32 vcc, v190, v210
	s_waitcnt lgkmcnt(0)
	v_and_b32_e32 v213, 0xffff0000, v250
	v_cndmask_b32_e32 v190, v244, v190, vcc
	v_lshlrev_b32_e32 v248, 2, v190
	v_xor_b32_e32 v190, 4, v244
	v_cmp_lt_i32_e32 vcc, v190, v210
	v_and_b32_e32 v217, 0xffff0000, v251
	v_lshlrev_b32_e32 v212, 16, v250
	v_cndmask_b32_e32 v190, v244, v190, vcc
	v_lshlrev_b32_e32 v216, 16, v251
	v_mul_f32_e32 v250, v213, v213
	v_mul_f32_e32 v251, v217, v217
	v_lshlrev_b32_e32 v202, 2, v190
	v_xor_b32_e32 v190, 8, v244
	v_and_b32_e32 v211, 0xffff0000, v252
	v_fmac_f32_e32 v250, v212, v212
	v_fmac_f32_e32 v251, v216, v216
	v_cmp_lt_i32_e32 vcc, v190, v210
	v_lshlrev_b32_e32 v210, 16, v252
	v_add_f32_e32 v250, v250, v251
	v_mul_f32_e32 v251, v211, v211
	v_and_b32_e32 v215, 0xffff0000, v253
	v_fmac_f32_e32 v251, v210, v210
	v_lshlrev_b32_e32 v214, 16, v253
	v_add_f32_e32 v250, v251, v250
	v_mul_f32_e32 v251, v215, v215
	v_fmac_f32_e32 v251, v214, v214
	v_add_f32_e32 v250, v251, v250
	ds_bpermute_b32 v251, v249, v250
	v_cndmask_b32_e32 v190, v244, v190, vcc
	v_lshlrev_b32_e32 v190, 2, v190
	s_waitcnt lgkmcnt(0)
	v_add_f32_e32 v250, v250, v251
	ds_bpermute_b32 v251, v248, v250
	s_waitcnt lgkmcnt(0)
	v_add_f32_e32 v250, v250, v251
	ds_bpermute_b32 v251, v202, v250
	s_waitcnt lgkmcnt(0)
	v_add_f32_e32 v250, v250, v251
	ds_bpermute_b32 v251, v190, v250
	s_and_saveexec_b64 s[64:65], s[26:27]
	s_cbranch_execz .LBB0_426
	s_waitcnt lgkmcnt(0)
	v_add_f32_e32 v252, v250, v251
	v_add_u32_e32 v250, s60, v219
	v_add_u32_e32 v250, s50, v250
	v_ashrrev_i32_e32 v251, 31, v250
	v_lshlrev_b64 v[250:251], 6, v[250:251]
	v_lshl_add_u64 v[250:251], s[62:63], 0, v[250:251]
	global_store_dword v[250:251], v252, off
; #define GAS __attribute__((address_space(1)))
; #define LAS __attribute__((address_space(3)))
; __device__ __forceinline__ f32x4 bf4lo(const v4u& w) { return (f32x4){bflo(w.x), bfhi(w.x), bflo(w.y), bfhi(w.y)}; }
; __device__ __forceinline__ f32x4 bf4hi(const v4u& w) { return (f32x4){bflo(w.z), bfhi(w.z), bflo(w.w), bfhi(w.w)}; }
; __device__ __forceinline__ unsigned cvtpk(float lo, float hi) { f32x2_t v = {lo, hi}; bf16x2_t b = __builtin_convertvector(v, bf16x2_t); return __builtin_bit_cast(unsigned, b); }
; template <int PASS> ...
;     ...
;             const f32x4 hw0 = *(const LAS f32x4*)(lds + MISC_OFF + 256 + (tid & 15) * 32), hw1 = *(const LAS f32x4*)(lds + MISC_OFF + 256 + (tid & 15) * 32 + 16);
; #pragma unroll
;             for (int i = 0; i < 2; ++i) { const int id = tid + 512 * i, row = id >> 4, cc = id & 15;
;                 const v4u ov = *(const LAS v4u*)(lds + OFF_O + row * OS + cc * 16);
;                 const f32x4 a = bf4lo(ov), b = bf4hi(ov), ga = bf4lo(gpre[i]), gb = bf4hi(gpre[i]);
;                 float ss = (a.x * a.x + a.y * a.y) + (a.z * a.z + a.w * a.w) + (b.x * b.x + b.y * b.y) + (b.z * b.z + b.w * b.w);
;                 ss += __shfl_xor(ss, 1); ss += __shfl_xor(ss, 2); ss += __shfl_xor(ss, 4); ss += __shfl_xor(ss, 8);
;                 if (cc == 0) SS[(size_t)(tok0 + row) * 16 + h * 4 + s] = ss;
;                 const f32x4 ya = a * ga * hw0, yb = b * gb * hw1;
;                 v4u o; o.x = cvtpk(ya.x, ya.y); o.y = cvtpk(ya.z, ya.w); o.z = cvtpk(yb.x, yb.y); o.w = cvtpk(yb.z, yb.w);
;                 *(GAS v4u*)((GAS char*)OG + (size_t)tok0 * VD * 2 + i * 32 * VD * 2 + voff) = o; }
;         }
;         if (c + 1 < CPP) {
;             if (PASS == 1) {
;                 if ((c & 1) == 0) { write_stage<NQ>(lds, st0, tid); if (c + 3 < CPP) issue_loads<NQ>(st0, QP, KP, VB, BC, tok0 + 3 * CHK, h, s, tid, qkoff, voff); }
;                 else { write_stage<NQ>(lds, st1, tid); if (c + 3 < CPP) issue_loads<NQ>(st1, QP, KP, VB, BC, tok0 + 3 * CHK, h, s, tid, qkoff, voff); }
;             } else { write_stage<NQ>(lds, st0, tid); if (c + 2 < CPP) issue_loads<NQ>(st0, QP, KP, VB, BC, tok0 + 2 * CHK, h, s, tid, qkoff, voff); }
.LBB0_426:
	s_or_b64 exec, exec, s[64:65]
	s_waitcnt vmcnt(1)
	v_lshlrev_b32_e32 v254, 4, v0
	v_add_u32_e32 v254, 0x1c000, v254
	ds_read_b128 v[146:149], v254
	s_waitcnt lgkmcnt(0)
	v_lshlrev_b32_e32 v250, 16, v146
	s_waitcnt lgkmcnt(0)
	v_and_b32_e32 v251, 0xffff0000, v146
	v_lshlrev_b32_e32 v146, 16, v147
	v_and_b32_e32 v147, 0xffff0000, v147
	v_pk_mul_f32 v[212:213], v[250:251], v[212:213]
	v_pk_mul_f32 v[146:147], v[146:147], v[216:217]
	v_lshlrev_b32_e32 v252, 16, v148
	v_and_b32_e32 v253, 0xffff0000, v148
	v_lshlrev_b32_e32 v148, 16, v149
	v_and_b32_e32 v149, 0xffff0000, v149
	v_pk_mul_f32 v[216:217], v[112:113], v[146:147]
	v_pk_mul_f32 v[146:147], v[110:111], v[212:213]
	v_pk_mul_f32 v[148:149], v[148:149], v[214:215]
	v_cvt_pk_bf16_f32 v146, v146, v147
	v_cvt_pk_bf16_f32 v147, v216, v217
	ds_read_b128 v[214:217], v234
	v_pk_mul_f32 v[210:211], v[252:253], v[210:211]
	v_pk_mul_f32 v[212:213], v[108:109], v[148:149]
	v_pk_mul_f32 v[148:149], v[106:107], v[210:211]
	v_add_co_u32_e32 v210, vcc, s90, v208
	v_cvt_pk_bf16_f32 v148, v148, v149
	v_cvt_pk_bf16_f32 v149, v212, v213
	v_addc_co_u32_e32 v211, vcc, -1, v209, vcc
	global_store_dwordx4 v[210:211], v[146:149], off
	s_waitcnt lgkmcnt(0)
	v_and_b32_e32 v213, 0xffff0000, v214
	v_and_b32_e32 v211, 0xffff0000, v215
	v_lshlrev_b32_e32 v212, 16, v214
	v_lshlrev_b32_e32 v210, 16, v215
	v_mul_f32_e32 v214, v213, v213
	v_mul_f32_e32 v215, v211, v211
	v_and_b32_e32 v149, 0xffff0000, v216
	v_fmac_f32_e32 v214, v212, v212
	v_fmac_f32_e32 v215, v210, v210
	v_lshlrev_b32_e32 v148, 16, v216
	v_add_f32_e32 v214, v214, v215
	v_mul_f32_e32 v215, v149, v149
	v_and_b32_e32 v147, 0xffff0000, v217
	v_fmac_f32_e32 v215, v148, v148
	v_lshlrev_b32_e32 v146, 16, v217
	v_add_f32_e32 v214, v215, v214
	v_mul_f32_e32 v215, v147, v147
	v_fmac_f32_e32 v215, v146, v146
	v_add_f32_e32 v214, v215, v214
	ds_bpermute_b32 v215, v249, v214
	s_waitcnt lgkmcnt(0)
	v_add_f32_e32 v214, v214, v215
	ds_bpermute_b32 v215, v248, v214
	s_waitcnt lgkmcnt(0)
	v_add_f32_e32 v214, v214, v215
	ds_bpermute_b32 v202, v202, v214
	s_waitcnt lgkmcnt(0)
	v_add_f32_e32 v202, v214, v202
	ds_bpermute_b32 v190, v190, v202
	s_and_saveexec_b64 s[64:65], s[26:27]
	s_cbranch_execz .LBB0_428
	s_waitcnt lgkmcnt(0)
	v_add_f32_e32 v190, v202, v190
	v_add_u32_e32 v202, s60, v220
	v_add_u32_e32 v214, s50, v202
	v_ashrrev_i32_e32 v215, 31, v214
	v_lshlrev_b64 v[214:215], 6, v[214:215]
	v_lshl_add_u64 v[214:215], s[62:63], 0, v[214:215]
	global_store_dword v[214:215], v190, off
.LBB0_428:
	s_or_b64 exec, exec, s[64:65]
	s_waitcnt vmcnt(1)
	v_lshlrev_b32_e32 v254, 4, v0
	v_add_u32_e32 v254, 0x1c000, v254
	ds_read_b128 v[126:129], v254 offset:8192
	s_waitcnt lgkmcnt(0)
	v_lshlrev_b32_e32 v214, 16, v126
	v_and_b32_e32 v215, 0xffff0000, v126
	v_lshlrev_b32_e32 v126, 16, v127
	v_and_b32_e32 v127, 0xffff0000, v127
	v_lshlrev_b32_e32 v216, 16, v128
	v_and_b32_e32 v217, 0xffff0000, v128
	v_lshlrev_b32_e32 v128, 16, v129
	v_and_b32_e32 v129, 0xffff0000, v129
	v_pk_mul_f32 v[126:127], v[126:127], v[210:211]
	v_pk_mul_f32 v[212:213], v[214:215], v[212:213]
	v_pk_mul_f32 v[112:113], v[112:113], v[126:127]
	v_pk_mul_f32 v[126:127], v[216:217], v[148:149]
	v_pk_mul_f32 v[128:129], v[128:129], v[146:147]
	v_pk_mul_f32 v[110:111], v[110:111], v[212:213]
	v_pk_mul_f32 v[128:129], v[108:109], v[128:129]
	v_pk_mul_f32 v[108:109], v[106:107], v[126:127]
	v_cvt_pk_bf16_f32 v106, v110, v111
	v_cvt_pk_bf16_f32 v107, v112, v113
	v_cvt_pk_bf16_f32 v108, v108, v109
	v_cvt_pk_bf16_f32 v109, v128, v129
	s_cmpk_eq_i32 s50, 0x3c0
	global_store_dwordx4 v[208:209], v[106:109], off
	s_cbranch_scc1 .LBB0_423
	ds_write_b128 v235, v[42:45]
	ds_write_b128 v236, v[46:49] offset:33792
	ds_write_b128 v237, v[50:53]
	ds_write_b128 v238, v[58:61] offset:33792
	ds_write_b128 v235, v[62:65] offset:16896
	ds_write_b128 v236, v[66:69] offset:51200
	ds_write_b128 v239, v[74:77]
	ds_write_b128 v240, v[78:81] offset:33792
	ds_write_b128 v241, v[82:85]
	ds_write_b128 v242, v[86:89]
	s_and_saveexec_b64 s[64:65], s[6:7]
	s_cbranch_execz .LBB0_431
	v_mul_f32_e32 v106, 0x3fb8aa3b, v247
	v_rndne_f32_e32 v107, v106
	v_sub_f32_e32 v108, v106, v107
	v_fma_f32 v106, v247, s85, -v106
	v_fmac_f32_e32 v106, 0x32a5705f, v247
	v_add_f32_e32 v106, v108, v106
	v_cvt_i32_f32_e32 v107, v107
	v_exp_f32_e32 v106, v106
	v_cmp_ngt_f32_e32 vcc, s86, v247
	v_ldexp_f32 v106, v106, v107
	s_nop 0
	v_cndmask_b32_e32 v106, 0, v106, vcc
	v_cmp_nlt_f32_e32 vcc, s87, v247
	s_nop 1
	v_cndmask_b32_e32 v106, v243, v106, vcc
	ds_write_b32 v245, v106
